# ticket order: conversion chunks dealt 25% ahead of the attention work (all chunks out before the last fifth of the units)
# baseline (speedup 1.0000x reference)
_ZN3attL9ATT_ORDERE:
	.short	8207
	.short	8206
	.short	8205
	.short	8204
	.short	8203
	.short	8202
	.short	8201
	.short	8200
	.short	8199
	.short	8198
	.short	8197
	.short	8196
	.short	8195
	.short	8194
	.short	8193
	.short	8271
	.short	8270
	.short	8269
	.short	8268
	.short	8267
	.short	8266
	.short	8265
	.short	8264
	.short	8263
	.short	8262
	.short	8261
	.short	8260
	.short	8259
	.short	8258
	.short	8257
	.short	8335
	.short	8334
	.short	8333
	.short	8332
	.short	8331
	.short	8330
	.short	8329
	.short	8328
	.short	8327
	.short	8326
	.short	8325
	.short	8324
	.short	8323
	.short	8322
	.short	8321
	.short	8399
	.short	8398
	.short	8397
	.short	8396
	.short	8395
	.short	8394
	.short	8393
	.short	8392
	.short	8391
	.short	8390
	.short	8389
	.short	8388
	.short	8387
	.short	8386
	.short	8385
	.short	8463
	.short	8462
	.short	8461
	.short	8460
	.short	8459
	.short	8458
	.short	8457
	.short	8456
	.short	8455
	.short	8454
	.short	8453
	.short	8452
	.short	8451
	.short	8450
	.short	8449
	.short	8719
	.short	8718
	.short	8717
	.short	8716
	.short	8715
	.short	8714
	.short	8713
	.short	8712
	.short	8711
	.short	8710
	.short	8709
	.short	8708
	.short	8707
	.short	8706
	.short	8705
	.short	8783
	.short	8782
	.short	8781
	.short	8780
	.short	8779
	.short	8778
	.short	8777
	.short	8776
	.short	8775
	.short	8774
	.short	8773
	.short	8772
	.short	8771
	.short	8770
	.short	8769
	.short	8847
	.short	8846
	.short	8845
	.short	8844
	.short	8843
	.short	8842
	.short	8841
	.short	8840
	.short	8839
	.short	8838
	.short	8837
	.short	8836
	.short	8835
	.short	8834
	.short	8833
	.short	8911
	.short	8910
	.short	8909
	.short	8908
	.short	8907
	.short	8906
	.short	8905
	.short	8904
	.short	8903
	.short	8902
	.short	8901
	.short	8900
	.short	8899
	.short	8898
	.short	8897
	.short	8975
	.short	8974
	.short	8973
	.short	8972
	.short	8971
	.short	8970
	.short	8969
	.short	8968
	.short	8967
	.short	8966
	.short	8965
	.short	8964
	.short	8963
	.short	8962
	.short	8961
	.short	2063
	.short	32768
	.short	32769
	.short	2127
	.short	32770
	.short	32771
	.short	32772
	.short	2191
	.short	32773
	.short	32774
	.short	32775
	.short	2255
	.short	32776
	.short	32777
	.short	2319
	.short	32778
	.short	32779
	.short	32780
	.short	2575
	.short	32781
	.short	32782
	.short	32783
	.short	2639
	.short	32784
	.short	32785
	.short	2703
	.short	32786
	.short	32787
	.short	32788
	.short	2767
	.short	32789
	.short	32790
	.short	32791
	.short	2831
	.short	32792
	.short	32793
	.short	2062
	.short	32794
	.short	32795
	.short	32796
	.short	2126
	.short	32797
	.short	32798
	.short	32799
	.short	2190
	.short	32800
	.short	32801
	.short	2254
	.short	32802
	.short	32803
	.short	32804
	.short	2318
	.short	32805
	.short	32806
	.short	32807
	.short	2574
	.short	32808
	.short	32809
	.short	32810
	.short	2638
	.short	32811
	.short	32812
	.short	2702
	.short	32813
	.short	32814
	.short	32815
	.short	2766
	.short	32816
	.short	32817
	.short	32818
	.short	2830
	.short	32819
	.short	32820
	.short	2061
	.short	32821
	.short	32822
	.short	32823
	.short	2125
	.short	32824
	.short	32825
	.short	32826
	.short	2189
	.short	32827
	.short	32828
	.short	2253
	.short	32829
	.short	32830
	.short	32831
	.short	2317
	.short	32832
	.short	32833
	.short	32834
	.short	2573
	.short	32835
	.short	32836
	.short	2637
	.short	32837
	.short	32838
	.short	32839
	.short	2701
	.short	32840
	.short	32841
	.short	32842
	.short	2765
	.short	32843
	.short	32844
	.short	32845
	.short	2829
	.short	32846
	.short	32847
	.short	2060
	.short	32848
	.short	32849
	.short	32850
	.short	2124
	.short	32851
	.short	32852
	.short	32853
	.short	2188
	.short	32854
	.short	32855
	.short	2252
	.short	32856
	.short	32857
	.short	32858
	.short	2316
	.short	32859
	.short	32860
	.short	32861
	.short	2572
	.short	32862
	.short	32863
	.short	2636
	.short	32864
	.short	32865
	.short	32866
	.short	2700
	.short	32867
	.short	32868
	.short	32869
	.short	2764
	.short	32870
	.short	32871
	.short	2828
	.short	32872
	.short	32873
	.short	32874
	.short	2059
	.short	32875
	.short	32876
	.short	32877
	.short	2123
	.short	32878
	.short	32879
	.short	32880
	.short	2187
	.short	32881
	.short	32882
	.short	2251
	.short	32883
	.short	32884
	.short	32885
	.short	2315
	.short	32886
	.short	32887
	.short	32888
	.short	2571
	.short	32889
	.short	32890
	.short	2635
	.short	32891
	.short	32892
	.short	32893
	.short	2699
	.short	32894
	.short	32895
	.short	32896
	.short	2763
	.short	32897
	.short	32898
	.short	2827
	.short	32899
	.short	32900
	.short	32901
	.short	2058
	.short	32902
	.short	32903
	.short	32904
	.short	2122
	.short	32905
	.short	32906
	.short	2186
	.short	32907
	.short	32908
	.short	32909
	.short	2250
	.short	32910
	.short	32911
	.short	32912
	.short	2314
	.short	32913
	.short	32914
	.short	32915
	.short	2570
	.short	32916
	.short	32917
	.short	2634
	.short	32918
	.short	32919
	.short	32920
	.short	2698
	.short	32921
	.short	32922
	.short	32923
	.short	2762
	.short	32924
	.short	32925
	.short	2826
	.short	32926
	.short	32927
	.short	32928
	.short	2057
	.short	32929
	.short	32930
	.short	32931
	.short	2121
	.short	32932
	.short	32933
	.short	2185
	.short	32934
	.short	32935
	.short	32936
	.short	2249
	.short	32937
	.short	32938
	.short	32939
	.short	2313
	.short	32940
	.short	32941
	.short	2569
	.short	32942
	.short	32943
	.short	32944
	.short	2633
	.short	32945
	.short	32946
	.short	32947
	.short	2697
	.short	32948
	.short	32949
	.short	32950
	.short	2761
	.short	32951
	.short	32952
	.short	2825
	.short	32953
	.short	32954
	.short	32955
	.short	2056
	.short	32956
	.short	32957
	.short	32958
	.short	2120
	.short	32959
	.short	32960
	.short	2184
	.short	32961
	.short	32962
	.short	32963
	.short	2248
	.short	32964
	.short	32965
	.short	32966
	.short	2312
	.short	32967
	.short	32968
	.short	2568
	.short	32969
	.short	32970
	.short	32971
	.short	2632
	.short	32972
	.short	32973
	.short	32974
	.short	2696
	.short	32975
	.short	32976
	.short	2760
	.short	32977
	.short	32978
	.short	32979
	.short	2824
	.short	32980
	.short	32981
	.short	32982
	.short	2055
	.short	32983
	.short	32984
	.short	32985
	.short	2119
	.short	32986
	.short	32987
	.short	2183
	.short	32988
	.short	32989
	.short	32990
	.short	2247
	.short	32991
	.short	32992
	.short	32993
	.short	2311
	.short	32994
	.short	32995
	.short	2567
	.short	32996
	.short	32997
	.short	32998
	.short	2631
	.short	32999
	.short	33000
	.short	33001
	.short	2695
	.short	33002
	.short	33003
	.short	2759
	.short	33004
	.short	33005
	.short	33006
	.short	2823
	.short	33007
	.short	33008
	.short	33009
	.short	2054
	.short	33010
	.short	33011
	.short	2118
	.short	33012
	.short	33013
	.short	33014
	.short	2182
	.short	33015
	.short	33016
	.short	33017
	.short	2246
	.short	33018
	.short	33019
	.short	33020
	.short	2310
	.short	33021
	.short	33022
	.short	2566
	.short	33023
	.short	33024
	.short	33025
	.short	2630
	.short	33026
	.short	33027
	.short	33028
	.short	2694
	.short	33029
	.short	33030
	.short	2758
	.short	33031
	.short	33032
	.short	33033
	.short	2822
	.short	33034
	.short	33035
	.short	33036
	.short	2053
	.short	33037
	.short	33038
	.short	2117
	.short	33039
	.short	33040
	.short	33041
	.short	2181
	.short	33042
	.short	33043
	.short	33044
	.short	2245
	.short	33045
	.short	33046
	.short	2309
	.short	33047
	.short	33048
	.short	33049
	.short	2565
	.short	33050
	.short	33051
	.short	33052
	.short	2629
	.short	33053
	.short	33054
	.short	33055
	.short	2693
	.short	33056
	.short	33057
	.short	2757
	.short	33058
	.short	33059
	.short	33060
	.short	2821
	.short	33061
	.short	33062
	.short	33063
	.short	2052
	.short	33064
	.short	33065
	.short	2116
	.short	33066
	.short	33067
	.short	33068
	.short	2180
	.short	33069
	.short	33070
	.short	33071
	.short	2244
	.short	33072
	.short	33073
	.short	2308
	.short	33074
	.short	33075
	.short	33076
	.short	2564
	.short	33077
	.short	33078
	.short	33079
	.short	2628
	.short	33080
	.short	33081
	.short	2692
	.short	33082
	.short	33083
	.short	33084
	.short	2756
	.short	33085
	.short	33086
	.short	33087
	.short	2820
	.short	33088
	.short	33089
	.short	33090
	.short	2051
	.short	33091
	.short	33092
	.short	2115
	.short	33093
	.short	33094
	.short	33095
	.short	2179
	.short	33096
	.short	33097
	.short	33098
	.short	2243
	.short	33099
	.short	33100
	.short	2307
	.short	33101
	.short	33102
	.short	33103
	.short	2563
	.short	33104
	.short	33105
	.short	33106
	.short	2627
	.short	33107
	.short	33108
	.short	2691
	.short	33109
	.short	33110
	.short	33111
	.short	2755
	.short	33112
	.short	33113
	.short	33114
	.short	2819
	.short	33115
	.short	33116
	.short	2050
	.short	33117
	.short	33118
	.short	33119
	.short	2114
	.short	33120
	.short	33121
	.short	33122
	.short	2178
	.short	33123
	.short	33124
	.short	33125
	.short	2242
	.short	33126
	.short	33127
	.short	2306
	.short	33128
	.short	33129
	.short	33130
	.short	2562
	.short	33131
	.short	33132
	.short	33133
	.short	2626
	.short	33134
	.short	33135
	.short	2690
	.short	33136
	.short	33137
	.short	33138
	.short	2754
	.short	33139
	.short	33140
	.short	33141
	.short	2818
	.short	33142
	.short	33143
	.short	2049
	.short	33144
	.short	33145
	.short	33146
	.short	2113
	.short	33147
	.short	33148
	.short	33149
	.short	2177
	.short	33150
	.short	33151
	.short	2241
	.short	33152
	.short	33153
	.short	33154
	.short	2305
	.short	33155
	.short	33156
	.short	33157
	.short	2561
	.short	33158
	.short	33159
	.short	33160
	.short	2625
	.short	33161
	.short	33162
	.short	2689
	.short	33163
	.short	33164
	.short	33165
	.short	2753
	.short	33166
	.short	33167
	.short	33168
	.short	2817
	.short	33169
	.short	33170
	.short	2048
	.short	33171
	.short	33172
	.short	2112
	.short	33173
	.short	33174
	.short	2176
	.short	33175
	.short	33176
	.short	2240
	.short	33177
	.short	2304
	.short	33178
	.short	33179
	.short	2560
	.short	33180
	.short	33181
	.short	2624
	.short	33182
	.short	33183
	.short	2688
	.short	33184
	.short	33185
	.short	2752
	.short	33186
	.short	2816
	.short	33187
	.short	33188
	.short	1039
	.short	33189
	.short	33190
	.short	1103
	.short	33191
	.short	33192
	.short	1167
	.short	33193
	.short	33194
	.short	1231
	.short	33195
	.short	1295
	.short	33196
	.short	33197
	.short	1551
	.short	33198
	.short	33199
	.short	1615
	.short	33200
	.short	33201
	.short	1679
	.short	33202
	.short	33203
	.short	1743
	.short	33204
	.short	1807
	.short	33205
	.short	33206
	.short	1038
	.short	33207
	.short	33208
	.short	1102
	.short	33209
	.short	33210
	.short	1166
	.short	33211
	.short	33212
	.short	1230
	.short	33213
	.short	1294
	.short	33214
	.short	33215
	.short	1550
	.short	33216
	.short	33217
	.short	1614
	.short	33218
	.short	33219
	.short	1678
	.short	33220
	.short	33221
	.short	1742
	.short	33222
	.short	1806
	.short	33223
	.short	33224
	.short	1037
	.short	33225
	.short	33226
	.short	1101
	.short	33227
	.short	33228
	.short	1165
	.short	33229
	.short	33230
	.short	1229
	.short	33231
	.short	1293
	.short	33232
	.short	33233
	.short	1549
	.short	33234
	.short	33235
	.short	1613
	.short	33236
	.short	33237
	.short	1677
	.short	33238
	.short	33239
	.short	1741
	.short	33240
	.short	1805
	.short	33241
	.short	33242
	.short	1036
	.short	33243
	.short	33244
	.short	1100
	.short	33245
	.short	33246
	.short	1164
	.short	33247
	.short	1228
	.short	33248
	.short	33249
	.short	1292
	.short	33250
	.short	33251
	.short	1548
	.short	33252
	.short	33253
	.short	1612
	.short	33254
	.short	33255
	.short	1676
	.short	33256
	.short	1740
	.short	33257
	.short	33258
	.short	1804
	.short	33259
	.short	33260
	.short	1035
	.short	33261
	.short	33262
	.short	1099
	.short	33263
	.short	33264
	.short	1163
	.short	33265
	.short	1227
	.short	33266
	.short	33267
	.short	1291
	.short	33268
	.short	33269
	.short	1547
	.short	33270
	.short	33271
	.short	1611
	.short	33272
	.short	33273
	.short	1675
	.short	33274
	.short	1739
	.short	33275
	.short	33276
	.short	1803
	.short	33277
	.short	33278
	.short	1034
	.short	33279
	.short	33280
	.short	1098
	.short	33281
	.short	33282
	.short	1162
	.short	33283
	.short	1226
	.short	33284
	.short	33285
	.short	1290
	.short	33286
	.short	33287
	.short	1546
	.short	33288
	.short	33289
	.short	1610
	.short	33290
	.short	33291
	.short	1674
	.short	33292
	.short	1738
	.short	33293
	.short	33294
	.short	1802
	.short	33295
	.short	33296
	.short	1033
	.short	33297
	.short	33298
	.short	1097
	.short	33299
	.short	33300
	.short	1161
	.short	33301
	.short	1225
	.short	33302
	.short	33303
	.short	1289
	.short	33304
	.short	33305
	.short	1545
	.short	33306
	.short	33307
	.short	1609
	.short	33308
	.short	1673
	.short	33309
	.short	33310
	.short	1737
	.short	33311
	.short	33312
	.short	1801
	.short	33313
	.short	33314
	.short	1032
	.short	33315
	.short	33316
	.short	1096
	.short	33317
	.short	1160
	.short	33318
	.short	33319
	.short	1224
	.short	33320
	.short	33321
	.short	1288
	.short	33322
	.short	33323
	.short	1544
	.short	33324
	.short	33325
	.short	1608
	.short	33326
	.short	1672
	.short	33327
	.short	33328
	.short	1736
	.short	33329
	.short	33330
	.short	1800
	.short	33331
	.short	33332
	.short	1031
	.short	33333
	.short	33334
	.short	1095
	.short	33335
	.short	1159
	.short	33336
	.short	33337
	.short	1223
	.short	33338
	.short	33339
	.short	1287
	.short	33340
	.short	33341
	.short	1543
	.short	33342
	.short	33343
	.short	1607
	.short	33344
	.short	1671
	.short	33345
	.short	33346
	.short	1735
	.short	33347
	.short	33348
	.short	1799
	.short	33349
	.short	33350
	.short	1030
	.short	33351
	.short	33352
	.short	1094
	.short	33353
	.short	1158
	.short	33354
	.short	33355
	.short	1222
	.short	33356
	.short	33357
	.short	1286
	.short	33358
	.short	33359
	.short	1542
	.short	33360
	.short	33361
	.short	1606
	.short	33362
	.short	1670
	.short	33363
	.short	33364
	.short	1734
	.short	33365
	.short	33366
	.short	1798
	.short	33367
	.short	33368
	.short	1029
	.short	33369
	.short	33370
	.short	1093
	.short	33371
	.short	1157
	.short	33372
	.short	33373
	.short	1221
	.short	33374
	.short	33375
	.short	1285
	.short	33376
	.short	33377
	.short	1541
	.short	33378
	.short	1605
	.short	33379
	.short	33380
	.short	1669
	.short	33381
	.short	33382
	.short	1733
	.short	33383
	.short	33384
	.short	1797
	.short	33385
	.short	33386
	.short	1028
	.short	33387
	.short	1092
	.short	33388
	.short	33389
	.short	1156
	.short	33390
	.short	33391
	.short	1220
	.short	33392
	.short	33393
	.short	1284
	.short	33394
	.short	33395
	.short	1540
	.short	33396
	.short	1604
	.short	33397
	.short	33398
	.short	1668
	.short	33399
	.short	33400
	.short	1732
	.short	33401
	.short	33402
	.short	1796
	.short	33403
	.short	33404
	.short	1027
	.short	33405
	.short	1091
	.short	33406
	.short	33407
	.short	1155
	.short	33408
	.short	33409
	.short	1219
	.short	33410
	.short	33411
	.short	1283
	.short	33412
	.short	33413
	.short	1539
	.short	33414
	.short	1603
	.short	33415
	.short	33416
	.short	1667
	.short	33417
	.short	33418
	.short	1731
	.short	33419
	.short	33420
	.short	1795
	.short	33421
	.short	33422
	.short	1026
	.short	33423
	.short	1090
	.short	33424
	.short	33425
	.short	1154
	.short	33426
	.short	33427
	.short	1218
	.short	33428
	.short	33429
	.short	1282
	.short	33430
	.short	33431
	.short	1538
	.short	33432
	.short	1602
	.short	33433
	.short	33434
	.short	1666
	.short	33435
	.short	33436
	.short	1730
	.short	33437
	.short	33438
	.short	1794
	.short	33439
	.short	33440
	.short	1025
	.short	33441
	.short	1089
	.short	33442
	.short	33443
	.short	1153
	.short	33444
	.short	33445
	.short	1217
	.short	33446
	.short	33447
	.short	1281
	.short	33448
	.short	1537
	.short	33449
	.short	33450
	.short	1601
	.short	33451
	.short	33452
	.short	1665
	.short	33453
	.short	33454
	.short	1729
	.short	33455
	.short	33456
	.short	1793
	.short	33457
	.short	1024
	.short	33458
	.short	33459
	.short	1088
	.short	33460
	.short	33461
	.short	1152
	.short	33462
	.short	33463
	.short	1216
	.short	33464
	.short	33465
	.short	1280
	.short	33466
	.short	1536
	.short	33467
	.short	33468
	.short	1600
	.short	33469
	.short	33470
	.short	1664
	.short	33471
	.short	33472
	.short	1728
	.short	33473
	.short	33474
	.short	1792
	.short	33475
	.short	47
	.short	33476
	.short	33477
	.short	111
	.short	33478
	.short	33479
	.short	175
	.short	33480
	.short	33481
	.short	239
	.short	33482
	.short	33483
	.short	303
	.short	33484
	.short	367
	.short	33485
	.short	33486
	.short	559
	.short	33487
	.short	33488
	.short	623
	.short	33489
	.short	33490
	.short	687
	.short	33491
	.short	33492
	.short	751
	.short	33493
	.short	815
	.short	33494
	.short	33495
	.short	879
	.short	33496
	.short	33497
	.short	46
	.short	33498
	.short	33499
	.short	110
	.short	33500
	.short	33501
	.short	174
	.short	33502
	.short	238
	.short	33503
	.short	33504
	.short	302
	.short	33505
	.short	33506
	.short	366
	.short	33507
	.short	33508
	.short	558
	.short	33509
	.short	33510
	.short	622
	.short	33511
	.short	686
	.short	33512
	.short	33513
	.short	750
	.short	33514
	.short	33515
	.short	814
	.short	33516
	.short	33517
	.short	878
	.short	33518
	.short	45
	.short	33519
	.short	33520
	.short	109
	.short	33521
	.short	33522
	.short	173
	.short	33523
	.short	33524
	.short	237
	.short	33525
	.short	33526
	.short	301
	.short	33527
	.short	365
	.short	33528
	.short	33529
	.short	557
	.short	33530
	.short	33531
	.short	621
	.short	33532
	.short	33533
	.short	685
	.short	33534
	.short	33535
	.short	749
	.short	33536
	.short	813
	.short	33537
	.short	33538
	.short	877
	.short	33539
	.short	33540
	.short	44
	.short	33541
	.short	33542
	.short	108
	.short	33543
	.short	33544
	.short	172
	.short	33545
	.short	236
	.short	33546
	.short	33547
	.short	300
	.short	33548
	.short	33549
	.short	364
	.short	33550
	.short	33551
	.short	556
	.short	33552
	.short	33553
	.short	620
	.short	33554
	.short	684
	.short	33555
	.short	33556
	.short	748
	.short	33557
	.short	33558
	.short	812
	.short	33559
	.short	33560
	.short	876
	.short	33561
	.short	33562
	.short	43
	.short	33563
	.short	107
	.short	33564
	.short	33565
	.short	171
	.short	33566
	.short	33567
	.short	235
	.short	33568
	.short	33569
	.short	299
	.short	33570
	.short	33571
	.short	363
	.short	33572
	.short	555
	.short	33573
	.short	33574
	.short	619
	.short	33575
	.short	33576
	.short	683
	.short	33577
	.short	33578
	.short	747
	.short	33579
	.short	811
	.short	33580
	.short	33581
	.short	875
	.short	33582
	.short	33583
	.short	42
	.short	33584
	.short	33585
	.short	106
	.short	33586
	.short	33587
	.short	170
	.short	33588
	.short	234
	.short	33589
	.short	33590
	.short	298
	.short	33591
	.short	33592
	.short	362
	.short	33593
	.short	33594
	.short	554
	.short	33595
	.short	33596
	.short	618
	.short	33597
	.short	682
	.short	33598
	.short	33599
	.short	746
	.short	33600
	.short	33601
	.short	810
	.short	33602
	.short	33603
	.short	874
	.short	33604
	.short	33605
	.short	41
	.short	33606
	.short	105
	.short	33607
	.short	33608
	.short	169
	.short	33609
	.short	33610
	.short	233
	.short	33611
	.short	33612
	.short	297
	.short	33613
	.short	33614
	.short	361
	.short	33615
	.short	553
	.short	33616
	.short	33617
	.short	617
	.short	33618
	.short	33619
	.short	681
	.short	33620
	.short	33621
	.short	745
	.short	33622
	.short	33623
	.short	809
	.short	33624
	.short	873
	.short	33625
	.short	33626
	.short	40
	.short	33627
	.short	33628
	.short	104
	.short	33629
	.short	33630
	.short	168
	.short	33631
	.short	33632
	.short	232
	.short	33633
	.short	296
	.short	33634
	.short	33635
	.short	360
	.short	33636
	.short	33637
	.short	552
	.short	33638
	.short	33639
	.short	616
	.short	33640
	.short	33641
	.short	680
	.short	33642
	.short	744
	.short	33643
	.short	33644
	.short	808
	.short	33645
	.short	33646
	.short	872
	.short	33647
	.short	33648
	.short	39
	.short	33649
	.short	103
	.short	33650
	.short	33651
	.short	167
	.short	33652
	.short	33653
	.short	231
	.short	33654
	.short	33655
	.short	295
	.short	33656
	.short	33657
	.short	359
	.short	33658
	.short	551
	.short	33659
	.short	33660
	.short	615
	.short	33661
	.short	33662
	.short	679
	.short	33663
	.short	33664
	.short	743
	.short	33665
	.short	33666
	.short	807
	.short	33667
	.short	871
	.short	33668
	.short	33669
	.short	38
	.short	33670
	.short	33671
	.short	102
	.short	33672
	.short	33673
	.short	166
	.short	33674
	.short	33675
	.short	230
	.short	33676
	.short	294
	.short	33677
	.short	33678
	.short	358
	.short	33679
	.short	33680
	.short	550
	.short	33681
	.short	33682
	.short	614
	.short	33683
	.short	33684
	.short	678
	.short	33685
	.short	742
	.short	33686
	.short	33687
	.short	806
	.short	33688
	.short	33689
	.short	870
	.short	33690
	.short	33691
	.short	37
	.short	33692
	.short	33693
	.short	101
	.short	33694
	.short	165
	.short	33695
	.short	33696
	.short	229
	.short	33697
	.short	33698
	.short	293
	.short	33699
	.short	33700
	.short	357
	.short	33701
	.short	33702
	.short	549
	.short	33703
	.short	613
	.short	33704
	.short	33705
	.short	677
	.short	33706
	.short	33707
	.short	741
	.short	33708
	.short	33709
	.short	805
	.short	33710
	.short	33711
	.short	869
	.short	33712
	.short	36
	.short	33713
	.short	33714
	.short	100
	.short	33715
	.short	33716
	.short	164
	.short	33717
	.short	33718
	.short	228
	.short	33719
	.short	292
	.short	33720
	.short	33721
	.short	356
	.short	33722
	.short	33723
	.short	548
	.short	33724
	.short	33725
	.short	612
	.short	33726
	.short	33727
	.short	676
	.short	33728
	.short	740
	.short	33729
	.short	33730
	.short	804
	.short	33731
	.short	33732
	.short	868
	.short	33733
	.short	33734
	.short	35
	.short	33735
	.short	33736
	.short	99
	.short	33737
	.short	163
	.short	33738
	.short	33739
	.short	227
	.short	33740
	.short	33741
	.short	291
	.short	33742
	.short	33743
	.short	355
	.short	33744
	.short	33745
	.short	547
	.short	33746
	.short	611
	.short	33747
	.short	33748
	.short	675
	.short	33749
	.short	33750
	.short	739
	.short	33751
	.short	33752
	.short	803
	.short	33753
	.short	33754
	.short	867
	.short	33755
	.short	34
	.short	33756
	.short	33757
	.short	98
	.short	33758
	.short	33759
	.short	162
	.short	33760
	.short	33761
	.short	226
	.short	33762
	.short	33763
	.short	290
	.short	33764
	.short	354
	.short	33765
	.short	33766
	.short	546
	.short	33767
	.short	33768
	.short	610
	.short	33769
	.short	33770
	.short	674
	.short	33771
	.short	33772
	.short	738
	.short	33773
	.short	802
	.short	33774
	.short	33775
	.short	866
	.short	33776
	.short	33777
	.short	33
	.short	33778
	.short	33779
	.short	97
	.short	33780
	.short	33781
	.short	161
	.short	33782
	.short	225
	.short	33783
	.short	33784
	.short	289
	.short	33785
	.short	33786
	.short	353
	.short	33787
	.short	33788
	.short	545
	.short	33789
	.short	609
	.short	33790
	.short	33791
	.short	673
	.short	33792
	.short	33793
	.short	737
	.short	33794
	.short	33795
	.short	801
	.short	33796
	.short	33797
	.short	865
	.short	33798
	.short	32
	.short	33799
	.short	33800
	.short	96
	.short	33801
	.short	33802
	.short	160
	.short	33803
	.short	33804
	.short	224
	.short	33805
	.short	33806
	.short	288
	.short	33807
	.short	352
	.short	33808
	.short	33809
	.short	544
	.short	33810
	.short	33811
	.short	608
	.short	33812
	.short	33813
	.short	672
	.short	33814
	.short	33815
	.short	736
	.short	33816
	.short	800
	.short	33817
	.short	33818
	.short	864
	.short	33819
	.short	33820
	.short	31
	.short	33821
	.short	33822
	.short	95
	.short	33823
	.short	33824
	.short	159
	.short	33825
	.short	223
	.short	33826
	.short	33827
	.short	287
	.short	33828
	.short	33829
	.short	351
	.short	33830
	.short	33831
	.short	543
	.short	33832
	.short	33833
	.short	607
	.short	33834
	.short	671
	.short	33835
	.short	33836
	.short	735
	.short	33837
	.short	33838
	.short	799
	.short	33839
	.short	33840
	.short	863
	.short	33841
	.short	33842
	.short	30
	.short	33843
	.short	94
	.short	33844
	.short	33845
	.short	158
	.short	33846
	.short	33847
	.short	222
	.short	33848
	.short	33849
	.short	286
	.short	33850
	.short	350
	.short	33851
	.short	33852
	.short	542
	.short	33853
	.short	33854
	.short	606
	.short	33855
	.short	33856
	.short	670
	.short	33857
	.short	33858
	.short	734
	.short	33859
	.short	798
	.short	33860
	.short	33861
	.short	862
	.short	33862
	.short	33863
	.short	29
	.short	33864
	.short	33865
	.short	93
	.short	33866
	.short	33867
	.short	157
	.short	33868
	.short	221
	.short	33869
	.short	33870
	.short	285
	.short	33871
	.short	33872
	.short	349
	.short	33873
	.short	33874
	.short	541
	.short	33875
	.short	33876
	.short	605
	.short	33877
	.short	669
	.short	33878
	.short	33879
	.short	733
	.short	33880
	.short	33881
	.short	797
	.short	33882
	.short	33883
	.short	861
	.short	33884
	.short	33885
	.short	28
	.short	33886
	.short	92
	.short	33887
	.short	33888
	.short	156
	.short	33889
	.short	33890
	.short	220
	.short	33891
	.short	33892
	.short	284
	.short	33893
	.short	33894
	.short	348
	.short	33895
	.short	540
	.short	33896
	.short	33897
	.short	604
	.short	33898
	.short	33899
	.short	668
	.short	33900
	.short	33901
	.short	732
	.short	33902
	.short	33903
	.short	796
	.short	33904
	.short	860
	.short	33905
	.short	33906
	.short	27
	.short	33907
	.short	33908
	.short	91
	.short	33909
	.short	33910
	.short	155
	.short	33911
	.short	33912
	.short	219
	.short	33913
	.short	283
	.short	33914
	.short	33915
	.short	347
	.short	33916
	.short	33917
	.short	539
	.short	33918
	.short	33919
	.short	603
	.short	33920
	.short	667
	.short	33921
	.short	33922
	.short	731
	.short	33923
	.short	33924
	.short	795
	.short	33925
	.short	33926
	.short	859
	.short	33927
	.short	33928
	.short	26
	.short	33929
	.short	90
	.short	33930
	.short	33931
	.short	154
	.short	33932
	.short	33933
	.short	218
	.short	33934
	.short	33935
	.short	282
	.short	33936
	.short	33937
	.short	346
	.short	33938
	.short	538
	.short	33939
	.short	33940
	.short	602
	.short	33941
	.short	33942
	.short	666
	.short	33943
	.short	33944
	.short	730
	.short	33945
	.short	33946
	.short	794
	.short	33947
	.short	858
	.short	33948
	.short	33949
	.short	25
	.short	33950
	.short	33951
	.short	89
	.short	33952
	.short	33953
	.short	153
	.short	33954
	.short	33955
	.short	217
	.short	33956
	.short	281
	.short	33957
	.short	33958
	.short	345
	.short	33959
	.short	33960
	.short	537
	.short	33961
	.short	33962
	.short	601
	.short	33963
	.short	33964
	.short	665
	.short	33965
	.short	729
	.short	33966
	.short	33967
	.short	793
	.short	33968
	.short	33969
	.short	857
	.short	33970
	.short	33971
	.short	24
	.short	33972
	.short	33973
	.short	88
	.short	33974
	.short	152
	.short	33975
	.short	33976
	.short	216
	.short	33977
	.short	33978
	.short	280
	.short	33979
	.short	33980
	.short	344
	.short	33981
	.short	33982
	.short	536
	.short	33983
	.short	600
	.short	33984
	.short	33985
	.short	664
	.short	33986
	.short	33987
	.short	728
	.short	33988
	.short	33989
	.short	792
	.short	33990
	.short	856
	.short	33991
	.short	33992
	.short	23
	.short	33993
	.short	33994
	.short	87
	.short	33995
	.short	33996
	.short	151
	.short	33997
	.short	33998
	.short	215
	.short	33999
	.short	279
	.short	34000
	.short	34001
	.short	343
	.short	34002
	.short	34003
	.short	535
	.short	34004
	.short	34005
	.short	599
	.short	34006
	.short	34007
	.short	663
	.short	34008
	.short	727
	.short	34009
	.short	34010
	.short	791
	.short	34011
	.short	34012
	.short	855
	.short	34013
	.short	34014
	.short	22
	.short	34015
	.short	34016
	.short	86
	.short	34017
	.short	150
	.short	34018
	.short	34019
	.short	214
	.short	34020
	.short	34021
	.short	278
	.short	34022
	.short	34023
	.short	342
	.short	34024
	.short	34025
	.short	534
	.short	34026
	.short	598
	.short	34027
	.short	34028
	.short	662
	.short	34029
	.short	34030
	.short	726
	.short	34031
	.short	34032
	.short	790
	.short	34033
	.short	34034
	.short	854
	.short	34035
	.short	21
	.short	34036
	.short	34037
	.short	85
	.short	34038
	.short	34039
	.short	149
	.short	34040
	.short	34041
	.short	213
	.short	34042
	.short	34043
	.short	277
	.short	34044
	.short	341
	.short	34045
	.short	34046
	.short	533
	.short	34047
	.short	34048
	.short	597
	.short	34049
	.short	34050
	.short	661
	.short	34051
	.short	34052
	.short	725
	.short	34053
	.short	789
	.short	34054
	.short	34055
	.short	853
	.short	34056
	.short	34057
	.short	20
	.short	34058
	.short	34059
	.short	84
	.short	34060
	.short	148
	.short	34061
	.short	34062
	.short	212
	.short	34063
	.short	34064
	.short	276
	.short	34065
	.short	34066
	.short	340
	.short	34067
	.short	34068
	.short	532
	.short	34069
	.short	596
	.short	34070
	.short	34071
	.short	660
	.short	34072
	.short	34073
	.short	724
	.short	34074
	.short	34075
	.short	788
	.short	34076
	.short	34077
	.short	852
	.short	34078
	.short	19
	.short	34079
	.short	34080
	.short	83
	.short	34081
	.short	34082
	.short	147
	.short	34083
	.short	34084
	.short	211
	.short	34085
	.short	34086
	.short	275
	.short	34087
	.short	339
	.short	34088
	.short	34089
	.short	531
	.short	34090
	.short	34091
	.short	595
	.short	34092
	.short	34093
	.short	659
	.short	34094
	.short	34095
	.short	723
	.short	34096
	.short	787
	.short	34097
	.short	34098
	.short	851
	.short	34099
	.short	34100
	.short	18
	.short	34101
	.short	34102
	.short	82
	.short	34103
	.short	34104
	.short	146
	.short	34105
	.short	210
	.short	34106
	.short	34107
	.short	274
	.short	34108
	.short	34109
	.short	338
	.short	34110
	.short	34111
	.short	530
	.short	34112
	.short	34113
	.short	594
	.short	34114
	.short	658
	.short	34115
	.short	34116
	.short	722
	.short	34117
	.short	34118
	.short	786
	.short	34119
	.short	34120
	.short	850
	.short	34121
	.short	17
	.short	34122
	.short	34123
	.short	81
	.short	34124
	.short	34125
	.short	145
	.short	34126
	.short	34127
	.short	209
	.short	34128
	.short	34129
	.short	273
	.short	34130
	.short	337
	.short	34131
	.short	34132
	.short	529
	.short	34133
	.short	34134
	.short	593
	.short	34135
	.short	34136
	.short	657
	.short	34137
	.short	34138
	.short	721
	.short	34139
	.short	785
	.short	34140
	.short	34141
	.short	849
	.short	34142
	.short	34143
	.short	16
	.short	34144
	.short	34145
	.short	80
	.short	34146
	.short	34147
	.short	144
	.short	34148
	.short	208
	.short	34149
	.short	34150
	.short	272
	.short	34151
	.short	34152
	.short	336
	.short	34153
	.short	34154
	.short	528
	.short	34155
	.short	34156
	.short	592
	.short	34157
	.short	656
	.short	34158
	.short	34159
	.short	720
	.short	34160
	.short	34161
	.short	784
	.short	34162
	.short	34163
	.short	848
	.short	34164
	.short	34165
	.short	15
	.short	34166
	.short	79
	.short	34167
	.short	34168
	.short	143
	.short	34169
	.short	34170
	.short	207
	.short	34171
	.short	34172
	.short	271
	.short	34173
	.short	34174
	.short	335
	.short	34175
	.short	527
	.short	34176
	.short	34177
	.short	591
	.short	34178
	.short	34179
	.short	655
	.short	34180
	.short	34181
	.short	719
	.short	34182
	.short	34183
	.short	783
	.short	34184
	.short	847
	.short	34185
	.short	34186
	.short	14
	.short	34187
	.short	34188
	.short	78
	.short	34189
	.short	34190
	.short	142
	.short	34191
	.short	206
	.short	34192
	.short	34193
	.short	270
	.short	34194
	.short	34195
	.short	334
	.short	34196
	.short	34197
	.short	526
	.short	34198
	.short	34199
	.short	590
	.short	34200
	.short	654
	.short	34201
	.short	34202
	.short	718
	.short	34203
	.short	34204
	.short	782
	.short	34205
	.short	34206
	.short	846
	.short	34207
	.short	34208
	.short	13
	.short	34209
	.short	77
	.short	34210
	.short	34211
	.short	141
	.short	34212
	.short	34213
	.short	205
	.short	34214
	.short	34215
	.short	269
	.short	34216
	.short	34217
	.short	333
	.short	34218
	.short	525
	.short	34219
	.short	34220
	.short	589
	.short	34221
	.short	34222
	.short	653
	.short	34223
	.short	34224
	.short	717
	.short	34225
	.short	34226
	.short	781
	.short	34227
	.short	845
	.short	34228
	.short	34229
	.short	12
	.short	34230
	.short	34231
	.short	76
	.short	34232
	.short	34233
	.short	140
	.short	34234
	.short	34235
	.short	204
	.short	34236
	.short	268
	.short	34237
	.short	34238
	.short	332
	.short	34239
	.short	34240
	.short	524
	.short	34241
	.short	34242
	.short	588
	.short	34243
	.short	34244
	.short	652
	.short	34245
	.short	716
	.short	34246
	.short	34247
	.short	780
	.short	34248
	.short	34249
	.short	844
	.short	34250
	.short	34251
	.short	11
	.short	34252
	.short	34253
	.short	75
	.short	34254
	.short	139
	.short	34255
	.short	34256
	.short	203
	.short	34257
	.short	34258
	.short	267
	.short	34259
	.short	34260
	.short	331
	.short	34261
	.short	523
	.short	34262
	.short	34263
	.short	587
	.short	34264
	.short	34265
	.short	651
	.short	34266
	.short	34267
	.short	715
	.short	34268
	.short	34269
	.short	779
	.short	34270
	.short	843
	.short	34271
	.short	34272
	.short	10
	.short	34273
	.short	34274
	.short	74
	.short	34275
	.short	34276
	.short	138
	.short	34277
	.short	34278
	.short	202
	.short	34279
	.short	266
	.short	34280
	.short	34281
	.short	330
	.short	34282
	.short	34283
	.short	522
	.short	34284
	.short	34285
	.short	586
	.short	34286
	.short	34287
	.short	650
	.short	34288
	.short	714
	.short	34289
	.short	34290
	.short	778
	.short	34291
	.short	34292
	.short	842
	.short	34293
	.short	34294
	.short	9
	.short	34295
	.short	34296
	.short	73
	.short	34297
	.short	137
	.short	34298
	.short	34299
	.short	201
	.short	34300
	.short	34301
	.short	265
	.short	34302
	.short	34303
	.short	329
	.short	34304
	.short	34305
	.short	521
	.short	34306
	.short	585
	.short	34307
	.short	34308
	.short	649
	.short	34309
	.short	34310
	.short	713
	.short	34311
	.short	34312
	.short	777
	.short	34313
	.short	34314
	.short	841
	.short	34315
	.short	8
	.short	34316
	.short	34317
	.short	72
	.short	34318
	.short	34319
	.short	136
	.short	34320
	.short	34321
	.short	200
	.short	34322
	.short	34323
	.short	264
	.short	34324
	.short	328
	.short	34325
	.short	34326
	.short	520
	.short	34327
	.short	34328
	.short	584
	.short	34329
	.short	34330
	.short	648
	.short	34331
	.short	712
	.short	34332
	.short	34333
	.short	776
	.short	34334
	.short	34335
	.short	840
	.short	34336
	.short	34337
	.short	7
	.short	34338
	.short	34339
	.short	71
	.short	34340
	.short	135
	.short	34341
	.short	34342
	.short	199
	.short	34343
	.short	34344
	.short	263
	.short	34345
	.short	34346
	.short	327
	.short	34347
	.short	34348
	.short	519
	.short	34349
	.short	583
	.short	34350
	.short	34351
	.short	647
	.short	34352
	.short	34353
	.short	711
	.short	34354
	.short	34355
	.short	775
	.short	34356
	.short	34357
	.short	839
	.short	34358
	.short	6
	.short	34359
	.short	34360
	.short	70
	.short	34361
	.short	34362
	.short	134
	.short	34363
	.short	34364
	.short	198
	.short	34365
	.short	34366
	.short	262
	.short	34367
	.short	326
	.short	34368
	.short	34369
	.short	518
	.short	34370
	.short	34371
	.short	582
	.short	34372
	.short	34373
	.short	646
	.short	34374
	.short	34375
	.short	710
	.short	34376
	.short	774
	.short	34377
	.short	34378
	.short	838
	.short	34379
	.short	34380
	.short	5
	.short	34381
	.short	34382
	.short	69
	.short	34383
	.short	34384
	.short	133
	.short	34385
	.short	197
	.short	34386
	.short	34387
	.short	261
	.short	34388
	.short	34389
	.short	325
	.short	34390
	.short	34391
	.short	517
	.short	34392
	.short	581
	.short	34393
	.short	34394
	.short	645
	.short	34395
	.short	34396
	.short	709
	.short	34397
	.short	34398
	.short	773
	.short	34399
	.short	34400
	.short	837
	.short	34401
	.short	4
	.short	34402
	.short	34403
	.short	68
	.short	34404
	.short	34405
	.short	132
	.short	34406
	.short	34407
	.short	196
	.short	34408
	.short	34409
	.short	260
	.short	34410
	.short	324
	.short	34411
	.short	34412
	.short	516
	.short	34413
	.short	34414
	.short	580
	.short	34415
	.short	34416
	.short	644
	.short	34417
	.short	34418
	.short	708
	.short	34419
	.short	772
	.short	34420
	.short	34421
	.short	836
	.short	34422
	.short	34423
	.short	3
	.short	34424
	.short	34425
	.short	67
	.short	34426
	.short	34427
	.short	131
	.short	34428
	.short	195
	.short	34429
	.short	34430
	.short	259
	.short	34431
	.short	34432
	.short	323
	.short	34433
	.short	34434
	.short	515
	.short	34435
	.short	34436
	.short	579
	.short	34437
	.short	643
	.short	34438
	.short	34439
	.short	707
	.short	34440
	.short	34441
	.short	771
	.short	34442
	.short	34443
	.short	835
	.short	34444
	.short	34445
	.short	2
	.short	34446
	.short	66
	.short	34447
	.short	34448
	.short	130
	.short	34449
	.short	34450
	.short	194
	.short	34451
	.short	34452
	.short	258
	.short	34453
	.short	34454
	.short	322
	.short	34455
	.short	514
	.short	34456
	.short	34457
	.short	578
	.short	34458
	.short	34459
	.short	642
	.short	34460
	.short	34461
	.short	706
	.short	34462
	.short	770
	.short	34463
	.short	34464
	.short	834
	.short	34465
	.short	34466
	.short	1
	.short	34467
	.short	34468
	.short	65
	.short	34469
	.short	34470
	.short	129
	.short	34471
	.short	193
	.short	34472
	.short	34473
	.short	257
	.short	34474
	.short	34475
	.short	321
	.short	34476
	.short	34477
	.short	513
	.short	34478
	.short	34479
	.short	577
	.short	34480
	.short	641
	.short	34481
	.short	34482
	.short	705
	.short	34483
	.short	34484
	.short	769
	.short	34485
	.short	34486
	.short	833
	.short	34487
	.short	34488
	.short	0
	.short	34489
	.short	64
	.short	34490
	.short	34491
	.short	128
	.short	34492
	.short	34493
	.short	192
	.short	34494
	.short	34495
	.short	256
	.short	34496
	.short	34497
	.short	320
	.short	34498
	.short	512
	.short	34499
	.short	34500
	.short	576
	.short	34501
	.short	34502
	.short	640
	.short	34503
	.short	34504
	.short	704
	.short	34505
	.short	34506
	.short	768
	.short	34507
	.short	832
	.short	34508
	.short	34509
	.short	16384
	.short	34510
	.short	34511
	.short	16640
	.short	34512
	.short	34513
	.short	16896
	.short	34514
	.short	34515
	.short	17152
	.short	34516
	.short	17408
	.short	34517
	.short	34518
	.short	18432
	.short	34519
	.short	34520
	.short	18688
	.short	34521
	.short	34522
	.short	18944
	.short	34523
	.short	34524
	.short	19200
	.short	34525
	.short	19456
	.short	34526
	.short	34527
	.short	16400
	.short	34528
	.short	34529
	.short	16656
	.short	34530
	.short	34531
	.short	16912
	.short	34532
	.short	17168
	.short	34533
	.short	34534
	.short	17424
	.short	34535
	.short	34536
	.short	18448
	.short	34537
	.short	34538
	.short	18704
	.short	34539
	.short	34540
	.short	18960
	.short	34541
	.short	19216
	.short	34542
	.short	34543
	.short	19472
	.short	34544
	.short	34545
	.short	16416
	.short	34546
	.short	34547
	.short	16672
	.short	34548
	.short	34549
	.short	16928
	.short	34550
	.short	17184
	.short	34551
	.short	34552
	.short	17440
	.short	34553
	.short	34554
	.short	18464
	.short	34555
	.short	34556
	.short	18720
	.short	34557
	.short	34558
	.short	18976
	.short	34559
	.short	19232
	.short	34560
	.short	34561
	.short	19488
	.short	34562
	.short	34563
	.short	16432
	.short	34564
	.short	34565
	.short	16688
	.short	34566
	.short	34567
	.short	16944
	.short	34568
	.short	17200
	.short	34569
	.short	34570
	.short	17456
	.short	34571
	.short	34572
	.short	18480
	.short	34573
	.short	34574
	.short	18736
	.short	34575
	.short	34576
	.short	18992
	.short	34577
	.short	19248
	.short	34578
	.short	34579
	.short	19504
	.short	34580
	.short	34581
	.short	16448
	.short	34582
	.short	34583
	.short	16704
	.short	34584
	.short	34585
	.short	16960
	.short	34586
	.short	17216
	.short	34587
	.short	34588
	.short	17472
	.short	34589
	.short	34590
	.short	18496
	.short	34591
	.short	34592
	.short	18752
	.short	34593
	.short	34594
	.short	19008
	.short	34595
	.short	19264
	.short	34596
	.short	34597
	.short	19520
	.short	34598
	.short	34599
	.short	16464
	.short	34600
	.short	34601
	.short	16720
	.short	34602
	.short	16976
	.short	34603
	.short	34604
	.short	17232
	.short	34605
	.short	34606
	.short	17488
	.short	34607
	.short	34608
	.short	18512
	.short	34609
	.short	34610
	.short	18768
	.short	34611
	.short	19024
	.short	34612
	.short	34613
	.short	19280
	.short	34614
	.short	34615
	.short	19536
	.short	34616
	.short	34617
	.short	16480
	.short	34618
	.short	34619
	.short	16736
	.short	34620
	.short	16992
	.short	34621
	.short	34622
	.short	17248
	.short	34623
	.short	34624
	.short	17504
	.short	34625
	.short	34626
	.short	18528
	.short	34627
	.short	34628
	.short	18784
	.short	34629
	.short	19040
	.short	34630
	.short	34631
	.short	19296
	.short	34632
	.short	34633
	.short	19552
	.short	34634
	.short	34635
	.short	16496
	.short	34636
	.short	34637
	.short	16752
	.short	34638
	.short	17008
	.short	34639
	.short	34640
	.short	17264
	.short	34641
	.short	34642
	.short	17520
	.short	34643
	.short	34644
	.short	18544
	.short	34645
	.short	34646
	.short	18800
	.short	34647
	.short	19056
	.short	34648
	.short	34649
	.short	19312
	.short	34650
	.short	34651
	.short	19568
	.short	34652
	.short	34653
	.short	16512
	.short	34654
	.short	34655
	.short	16768
	.short	34656
	.short	17024
	.short	34657
	.short	34658
	.short	17280
	.short	34659
	.short	34660
	.short	17536
	.short	34661
	.short	34662
	.short	18560
	.short	34663
	.short	18816
	.short	34664
	.short	34665
	.short	19072
	.short	34666
	.short	34667
	.short	19328
	.short	34668
	.short	34669
	.short	19584
	.short	34670
	.short	34671
	.short	16528
	.short	34672
	.short	16784
	.short	34673
	.short	34674
	.short	17040
	.short	34675
	.short	34676
	.short	17296
	.short	34677
	.short	34678
	.short	17552
	.short	34679
	.short	34680
	.short	18576
	.short	34681
	.short	18832
	.short	34682
	.short	34683
	.short	19088
	.short	34684
	.short	34685
	.short	19344
	.short	34686
	.short	34687
	.short	19600
	.short	34688
	.short	34689
	.short	16544
	.short	34690
	.short	16800
	.short	34691
	.short	34692
	.short	17056
	.short	34693
	.short	34694
	.short	17312
	.short	34695
	.short	34696
	.short	17568
	.short	34697
	.short	34698
	.short	18592
	.short	34699
	.short	18848
	.short	34700
	.short	34701
	.short	19104
	.short	34702
	.short	34703
	.short	19360
	.short	34704
	.short	34705
	.short	19616
	.short	34706
	.short	34707
	.short	16560
	.short	34708
	.short	16816
	.short	34709
	.short	34710
	.short	17072
	.short	34711
	.short	34712
	.short	17328
	.short	34713
	.short	34714
	.short	17584
	.short	34715
	.short	34716
	.short	18608
	.short	34717
	.short	18864
	.short	34718
	.short	34719
	.short	19120
	.short	34720
	.short	34721
	.short	19376
	.short	34722
	.short	34723
	.short	19632
	.short	34724
	.short	34725
	.short	16576
	.short	34726
	.short	16832
	.short	34727
	.short	34728
	.short	17088
	.short	34729
	.short	34730
	.short	17344
	.short	34731
	.short	34732
	.short	17600
	.short	34733
	.short	18624
	.short	34734
	.short	34735
	.short	18880
	.short	34736
	.short	34737
	.short	19136
	.short	34738
	.short	34739
	.short	19392
	.short	34740
	.short	34741
	.short	19648
	.short	34742
	.short	16592
	.short	34743
	.short	34744
	.short	16848
	.short	34745
	.short	34746
	.short	17104
	.short	34747
	.short	34748
	.short	17360
	.short	34749
	.short	34750
	.short	17616
	.short	34751
	.short	18640
	.short	34752
	.short	34753
	.short	18896
	.short	34754
	.short	34755
	.short	19152
	.short	34756
	.short	34757
	.short	19408
	.short	34758
	.short	34759
	.short	19664
	.short	34760
	.short	16608
	.short	34761
	.short	34762
	.short	16864
	.short	34763
	.short	34764
	.short	17120
	.short	34765
	.short	34766
	.short	17376
	.short	34767
	.short	34768
	.short	17632
	.short	34769
	.short	18656
	.short	34770
	.short	34771
	.short	18912
	.short	34772
	.short	34773
	.short	19168
	.short	34774
	.short	34775
	.short	19424
	.short	34776
	.short	34777
	.short	19680
	.short	34778
	.short	16385
	.short	34779
	.short	34780
	.short	16641
	.short	34781
	.short	34782
	.short	16897
	.short	34783
	.short	34784
	.short	17153
	.short	34785
	.short	34786
	.short	17409
	.short	34787
	.short	18433
	.short	34788
	.short	34789
	.short	18689
	.short	34790
	.short	34791
	.short	18945
	.short	34792
	.short	34793
	.short	19201
	.short	34794
	.short	34795
	.short	19457
	.short	34796
	.short	16401
	.short	34797
	.short	34798
	.short	16657
	.short	34799
	.short	34800
	.short	16913
	.short	34801
	.short	34802
	.short	17169
	.short	34803
	.short	17425
	.short	34804
	.short	34805
	.short	18449
	.short	34806
	.short	34807
	.short	18705
	.short	34808
	.short	34809
	.short	18961
	.short	34810
	.short	34811
	.short	19217
	.short	34812
	.short	19473
	.short	34813
	.short	34814
	.short	16417
	.short	34815
	.short	34816
	.short	16673
	.short	34817
	.short	34818
	.short	16929
	.short	34819
	.short	34820
	.short	17185
	.short	34821
	.short	17441
	.short	34822
	.short	34823
	.short	18465
	.short	34824
	.short	34825
	.short	18721
	.short	34826
	.short	34827
	.short	18977
	.short	34828
	.short	34829
	.short	19233
	.short	34830
	.short	19489
	.short	34831
	.short	34832
	.short	16433
	.short	34833
	.short	34834
	.short	16689
	.short	34835
	.short	34836
	.short	16945
	.short	34837
	.short	34838
	.short	17201
	.short	34839
	.short	17457
	.short	34840
	.short	34841
	.short	18481
	.short	34842
	.short	34843
	.short	18737
	.short	34844
	.short	34845
	.short	18993
	.short	34846
	.short	34847
	.short	19249
	.short	34848
	.short	19505
	.short	34849
	.short	34850
	.short	16449
	.short	34851
	.short	34852
	.short	16705
	.short	34853
	.short	34854
	.short	16961
	.short	34855
	.short	34856
	.short	17217
	.short	34857
	.short	17473
	.short	34858
	.short	34859
	.short	18497
	.short	34860
	.short	34861
	.short	18753
	.short	34862
	.short	34863
	.short	19009
	.short	34864
	.short	34865
	.short	19265
	.short	34866
	.short	19521
	.short	34867
	.short	34868
	.short	16465
	.short	34869
	.short	34870
	.short	16721
	.short	34871
	.short	34872
	.short	16977
	.short	34873
	.short	17233
	.short	34874
	.short	34875
	.short	17489
	.short	34876
	.short	34877
	.short	18513
	.short	34878
	.short	34879
	.short	18769
	.short	19025
	.short	19281
	.short	19537
	.short	16481
	.short	16737
	.short	16993
	.short	17249
	.short	17505
	.short	18529
	.short	18785
	.short	19041
	.short	19297
	.short	19553
	.short	16497
	.short	16753
	.short	17009
	.short	17265
	.short	17521
	.short	18545
	.short	18801
	.short	19057
	.short	19313
	.short	19569
	.short	16513
	.short	16769
	.short	17025
	.short	17281
	.short	17537
	.short	18561
	.short	18817
	.short	19073
	.short	19329
	.short	19585
	.short	16529
	.short	16785
	.short	17041
	.short	17297
	.short	17553
	.short	18577
	.short	18833
	.short	19089
	.short	19345
	.short	19601
	.short	16545
	.short	16801
	.short	17057
	.short	17313
	.short	17569
	.short	18593
	.short	18849
	.short	19105
	.short	19361
	.short	19617
	.short	16386
	.short	16642
	.short	16898
	.short	17154
	.short	17410
	.short	18434
	.short	18690
	.short	18946
	.short	19202
	.short	19458
	.short	16402
	.short	16658
	.short	16914
	.short	17170
	.short	17426
	.short	18450
	.short	18706
	.short	18962
	.short	19218
	.short	19474
	.short	16418
	.short	16674
	.short	16930
	.short	17186
	.short	17442
	.short	18466
	.short	18722
	.short	18978
	.short	19234
	.short	19490
	.short	16434
	.short	16690
	.short	16946
	.short	17202
	.short	17458
	.short	18482
	.short	18738
	.short	18994
	.short	19250
	.short	19506
	.short	16450
	.short	16706
	.short	16962
	.short	17218
	.short	17474
	.short	18498
	.short	18754
	.short	19010
	.short	19266
	.short	19522
	.short	16466
	.short	16722
	.short	16978
	.short	17234
	.short	17490
	.short	18514
	.short	18770
	.short	19026
	.short	19282
	.short	19538
	.short	16482
	.short	16738
	.short	16994
	.short	17250
	.short	17506
	.short	18530
	.short	18786
	.short	19042
	.short	19298
	.short	19554
	.short	16498
	.short	16754
	.short	17010
	.short	17266
	.short	17522
	.short	18546
	.short	18802
	.short	19058
	.short	19314
	.short	19570
	.short	16387
	.short	16643
	.short	16899
	.short	17155
	.short	17411
	.short	18435
	.short	18691
	.short	18947
	.short	19203
	.short	19459
	.short	16403
	.short	16659
	.short	16915
	.short	17171
	.short	17427
	.short	18451
	.short	18707
	.short	18963
	.short	19219
	.short	19475
	.short	16419
	.short	16675
	.short	16931
	.short	17187
	.short	17443
	.short	18467
	.short	18723
	.short	18979
	.short	19235
	.short	19491
	.short	16435
	.short	16691
	.short	16947
	.short	17203
	.short	17459
	.short	18483
	.short	18739
	.short	18995
	.short	19251
	.short	19507
	.short	16451
	.short	16707
	.short	16963
	.short	17219
	.short	17475
	.short	18499
	.short	18755
	.short	19011
	.short	19267
	.short	19523
	.short	16467
	.short	16723
	.short	16979
	.short	17235
	.short	17491
	.short	18515
	.short	18771
	.short	19027
	.short	19283
	.short	19539
	.short	16388
	.short	16644
	.short	16900
	.short	17156
	.short	17412
	.short	18436
	.short	18692
	.short	18948
	.short	19204
	.short	19460
	.short	16404
	.short	16660
	.short	16916
	.short	17172
	.short	17428
	.short	18452
	.short	18708
	.short	18964
	.short	19220
	.short	19476
	.short	16420
	.short	16676
	.short	16932
	.short	17188
	.short	17444
	.short	18468
	.short	18724
	.short	18980
	.short	19236
	.short	19492
	.short	16436
	.short	16692
	.short	16948
	.short	17204
	.short	17460
	.short	18484
	.short	18740
	.short	18996
	.short	19252
	.short	19508
	.short	16389
	.short	16645
	.short	16901
	.short	17157
	.short	17413
	.short	18437
	.short	18693
	.short	18949
	.short	19205
	.short	19461
	.short	16405
	.short	16661
	.short	16917
	.short	17173
	.short	17429
	.short	18453
	.short	18709
	.short	18965
	.short	19221
	.short	19477
	.short	16421
	.short	16677
	.short	16933
	.short	17189
	.short	17445
	.short	18469
	.short	18725
	.short	18981
	.short	19237
	.short	19493
	.short	16390
	.short	16646
	.short	16902
	.short	17158
	.short	17414
	.short	18438
	.short	18694
	.short	18950
	.short	19206
	.short	19462
	.short	16406
	.short	16662
	.short	16918
	.short	17174
	.short	17430
	.short	18454
	.short	18710
	.short	18966
	.short	19222
	.short	19478
	.short	16391
	.short	16647
	.short	16903
	.short	17159
	.short	17415
	.short	18439
	.short	18695
	.short	18951
	.short	19207
	.short	19463
	.short	20657
	.short	20913
	.short	21169
	.short	21425
	.short	21681
	.short	22705
	.short	22961
	.short	23217
	.short	23473
	.short	23729
	.short	20673
	.short	20929
	.short	21185
	.short	21441
	.short	21697
	.short	22721
	.short	22977
	.short	23233
	.short	23489
	.short	23745
	.short	20689
	.short	20945
	.short	21201
	.short	21457
	.short	21713
	.short	22737
	.short	22993
	.short	23249
	.short	23505
	.short	23761
	.short	20610
	.short	20866
	.short	21122
	.short	21378
	.short	21634
	.short	22658
	.short	22914
	.short	23170
	.short	23426
	.short	23682
	.short	20626
	.short	20882
	.short	21138
	.short	21394
	.short	21650
	.short	22674
	.short	22930
	.short	23186
	.short	23442
	.short	23698
	.short	20642
	.short	20898
	.short	21154
	.short	21410
	.short	21666
	.short	22690
	.short	22946
	.short	23202
	.short	23458
	.short	23714
	.short	20579
	.short	20835
	.short	21091
	.short	21347
	.short	21603
	.short	22627
	.short	22883
	.short	23139
	.short	23395
	.short	23651
	.short	20595
	.short	20851
	.short	21107
	.short	21363
	.short	21619
	.short	22643
	.short	22899
	.short	23155
	.short	23411
	.short	23667
	.short	20548
	.short	20804
	.short	21060
	.short	21316
	.short	21572
	.short	22596
	.short	22852
	.short	23108
	.short	23364
	.short	23620
	.short	20564
	.short	20820
	.short	21076
	.short	21332
	.short	21588
	.short	22612
	.short	22868
	.short	23124
	.short	23380
	.short	23636
	.short	20533
	.short	20789
	.short	21045
	.short	21301
	.short	21557
	.short	22581
	.short	22837
	.short	23093
	.short	23349
	.short	23605
	.short	20518
	.short	20774
	.short	21030
	.short	21286
	.short	21542
	.short	22566
	.short	22822
	.short	23078
	.short	23334
	.short	23590
	.short	20503
	.short	20759
	.short	21015
	.short	21271
	.short	21527
	.short	22551
	.short	22807
	.short	23063
	.short	23319
	.short	23575
	.short	20488
	.short	20744
	.short	21000
	.short	21256
	.short	21512
	.short	22536
	.short	22792
	.short	23048
	.short	23304
	.short	23560
	.size	_ZN3attL9ATT_ORDERE, 7596

	.type	__hip_cuid_5ba2c1623d679635,@object
